# speedup vs baseline: 1.0268x; 1.0268x over previous
.LBB4_10:
	v_ashrrev_i32_e32 v100, 2, v98
	v_and_b32_e32 v100, 0xffffffe0, v100
	v_add_u32_e32 v100, s38, v100
	v_lshrrev_b32_e32 v101, 2, v98
	v_and_or_b32 v112, v101, 12, v100
	v_ashrrev_i32_e32 v100, 2, v112
	v_ashrrev_i32_e32 v101, 31, v100
	v_lshlrev_b64 v[100:101], 2, v[100:101]
	v_lshl_add_u64 v[102:103], s[14:15], 0, v[100:101]
	v_add_co_u32_e32 v104, vcc, s11, v102
	v_lshl_add_u64 v[100:101], s[6:7], 0, v[100:101]
	s_nop 0
	v_addc_co_u32_e32 v105, vcc, 0, v103, vcc
	v_add_co_u32_e32 v106, vcc, s11, v100
	global_load_dword v146, v[102:103], off
	global_load_dword v226, v[102:103], off offset:16
	global_load_dword v234, v[102:103], off offset:128
	global_load_dword v242, v[102:103], off offset:144
	s_nop 0
	v_addc_co_u32_e32 v107, vcc, 0, v101, vcc
	v_add_co_u32_e32 v102, vcc, s35, v102
	global_load_dword v148, v[100:101], off
	global_load_dword v228, v[100:101], off offset:16
	global_load_dword v236, v[100:101], off offset:128
	global_load_dword v244, v[100:101], off offset:144
	s_nop 0
	v_addc_co_u32_e32 v103, vcc, 0, v103, vcc
	v_add_co_u32_e32 v100, vcc, s35, v100
	global_load_dword v147, v[104:105], off offset:-4096
	global_load_dword v227, v[104:105], off offset:-4080
	global_load_dword v235, v[104:105], off offset:-3968
	global_load_dword v243, v[104:105], off offset:-3952
	global_load_dword v150, v[104:105], off
	global_load_dword v230, v[104:105], off offset:16
	global_load_dword v238, v[104:105], off offset:128
	global_load_dword v246, v[104:105], off offset:144
	global_load_dword v149, v[106:107], off offset:-4096
	global_load_dword v229, v[106:107], off offset:-4080
	global_load_dword v237, v[106:107], off offset:-3968
	global_load_dword v245, v[106:107], off offset:-3952
	global_load_dword v152, v[106:107], off
	global_load_dword v232, v[106:107], off offset:16
	global_load_dword v240, v[106:107], off offset:128
	global_load_dword v248, v[106:107], off offset:144
	v_addc_co_u32_e32 v101, vcc, 0, v101, vcc
	global_load_dword v151, v[102:103], off
	global_load_dword v231, v[102:103], off offset:16
	global_load_dword v239, v[102:103], off offset:128
	global_load_dword v247, v[102:103], off offset:144
	global_load_dword v153, v[100:101], off
	global_load_dword v233, v[100:101], off offset:16
	global_load_dword v241, v[100:101], off offset:128
	global_load_dword v249, v[100:101], off offset:144
	v_and_b32_e32 v100, 15, v98
	v_bfe_i32 v98, v98, 6, 1
	v_and_b32_e32 v98, 48, v98
	v_or3_b32 v98, v100, v98, s37
	v_lshlrev_b64 v[100:101], 14, v[98:99]
	v_add_u32_e32 v102, 16, v98
	v_add_u32_e32 v104, 32, v98
	v_add_u32_e32 v106, 0x60, v98
	v_add_u32_e32 v108, 0x70, v98
	v_add_u32_e32 v98, 0x80, v98
	v_lshlrev_b64 v[110:111], 14, v[98:99]
	v_or_b32_e32 v98, 16, v112
	v_ashrrev_i32_e32 v156, 2, v98
	v_ashrrev_i32_e32 v157, 31, v156
	v_lshlrev_b64 v[156:157], 2, v[156:157]
	v_ashrrev_i32_e32 v113, 31, v112
	v_lshl_add_u64 v[168:169], s[14:15], 0, v[156:157]
	v_mov_b32_e32 v103, v99
	v_mov_b32_e32 v105, v99
	v_mov_b32_e32 v107, v99
	v_mov_b32_e32 v109, v99
	v_lshl_add_u64 v[154:155], v[112:113], 2, s[12:13]
	v_add_co_u32_e32 v170, vcc, s11, v168
	v_lshlrev_b64 v[102:103], 14, v[102:103]
	v_lshlrev_b64 v[104:105], 14, v[104:105]
	v_lshlrev_b64 v[106:107], 14, v[106:107]
	v_lshlrev_b64 v[108:109], 14, v[108:109]
	v_lshl_add_u64 v[158:159], v[154:155], 0, v[100:101]
	v_lshl_add_u64 v[156:157], s[6:7], 0, v[156:157]
	v_addc_co_u32_e32 v171, vcc, 0, v169, vcc
	v_lshl_add_u64 v[160:161], v[154:155], 0, v[102:103]
	v_lshl_add_u64 v[162:163], v[154:155], 0, v[104:105]
	v_lshl_add_u64 v[164:165], v[154:155], 0, v[106:107]
	v_lshl_add_u64 v[166:167], v[154:155], 0, v[108:109]
	v_lshl_add_u64 v[154:155], v[154:155], 0, v[110:111]
	s_waitcnt vmcnt(0)
	v_pk_add_f32 v[146:147], v[146:147], v[148:149]
	s_nop 0
	v_pk_add_f32 v[74:75], v[146:147], v[74:75]
	v_pk_add_f32 v[78:79], v[146:147], v[78:79]
	v_pk_add_f32 v[82:83], v[146:147], v[82:83]
	v_pk_add_f32 v[86:87], v[146:147], v[86:87]
	s_waitcnt vmcnt(0)
	v_pk_add_f32 v[148:149], v[150:151], v[152:153]
	v_pk_add_f32 v[90:91], v[146:147], v[90:91]
	v_pk_add_f32 v[76:77], v[148:149], v[76:77]
	v_pk_add_f32 v[94:95], v[146:147], v[94:95]
	v_pk_add_f32 v[80:81], v[148:149], v[80:81]
	v_pk_add_f32 v[84:85], v[148:149], v[84:85]
	v_pk_add_f32 v[88:89], v[148:149], v[88:89]
	v_pk_add_f32 v[92:93], v[148:149], v[92:93]
	v_pk_add_f32 v[96:97], v[148:149], v[96:97]
	global_store_dwordx4 v[158:159], v[74:77], off
	global_store_dwordx4 v[160:161], v[78:81], off
	global_store_dwordx4 v[162:163], v[82:85], off
	global_store_dwordx4 v[164:165], v[86:89], off
	global_store_dwordx4 v[166:167], v[90:93], off
	global_store_dwordx4 v[154:155], v[94:97], off
	v_add_co_u32_e32 v78, vcc, s11, v156
	v_mov_b32_e32 v74, v226
	v_mov_b32_e32 v76, v228
	v_addc_co_u32_e32 v79, vcc, 0, v157, vcc
	v_add_co_u32_e32 v82, vcc, s35, v168
	v_mov_b32_e32 v75, v227
	v_mov_b32_e32 v80, v230
	v_mov_b32_e32 v77, v229
	s_nop 0
	v_mov_b32_e32 v78, v232
	v_addc_co_u32_e32 v83, vcc, 0, v169, vcc
	v_mov_b32_e32 v81, v231
	v_add_co_u32_e32 v82, vcc, s35, v156
	v_pk_add_f32 v[74:75], v[74:75], v[76:77]
	v_addc_co_u32_e32 v83, vcc, 0, v157, vcc
	v_mov_b32_e32 v79, v233
	v_add_u32_e32 v82, 0x80, v112
	v_ashrrev_i32_e32 v84, 2, v82
	v_ashrrev_i32_e32 v85, 31, v84
	v_lshlrev_b64 v[84:85], 2, v[84:85]
	v_lshl_add_u64 v[86:87], s[14:15], 0, v[84:85]
	v_add_co_u32_e32 v88, vcc, s11, v86
	v_lshl_add_u64 v[84:85], s[6:7], 0, v[84:85]
	s_nop 0
	v_addc_co_u32_e32 v89, vcc, 0, v87, vcc
	v_add_co_u32_e32 v90, vcc, s11, v84
	v_pk_add_f32 v[50:51], v[74:75], v[50:51]
	s_nop 0
	v_addc_co_u32_e32 v91, vcc, 0, v85, vcc
	v_add_co_u32_e32 v92, vcc, s35, v86
	v_pk_add_f32 v[54:55], v[74:75], v[54:55]
	s_nop 0
	v_addc_co_u32_e32 v93, vcc, 0, v87, vcc
	v_add_co_u32_e32 v94, vcc, s35, v84
	v_pk_add_f32 v[58:59], v[74:75], v[58:59]
	v_pk_add_f32 v[62:63], v[74:75], v[62:63]
	v_pk_add_f32 v[66:67], v[74:75], v[66:67]
	v_pk_add_f32 v[70:71], v[74:75], v[70:71]
	v_addc_co_u32_e32 v95, vcc, 0, v85, vcc
	v_ashrrev_i32_e32 v83, 31, v82
	v_pk_add_f32 v[76:77], v[80:81], v[78:79]
	s_nop 0
	v_pk_add_f32 v[52:53], v[76:77], v[52:53]
	v_pk_add_f32 v[56:57], v[76:77], v[56:57]
	v_pk_add_f32 v[60:61], v[76:77], v[60:61]
	v_pk_add_f32 v[64:65], v[76:77], v[64:65]
	v_pk_add_f32 v[68:69], v[76:77], v[68:69]
	v_pk_add_f32 v[72:73], v[76:77], v[72:73]
	global_store_dwordx4 v[158:159], v[50:53], off offset:64
	global_store_dwordx4 v[160:161], v[54:57], off offset:64
	global_store_dwordx4 v[162:163], v[58:61], off offset:64
	global_store_dwordx4 v[164:165], v[62:65], off offset:64
	global_store_dwordx4 v[166:167], v[66:69], off offset:64
	global_store_dwordx4 v[154:155], v[70:73], off offset:64
	v_mov_b32_e32 v50, v234
	v_mov_b32_e32 v52, v236
	v_mov_b32_e32 v51, v235
	v_mov_b32_e32 v54, v238
	v_mov_b32_e32 v53, v237
	v_mov_b32_e32 v56, v240
	v_mov_b32_e32 v55, v239
	v_mov_b32_e32 v57, v241
	v_add_u32_e32 v58, 0x90, v112
	v_ashrrev_i32_e32 v60, 2, v58
	v_ashrrev_i32_e32 v61, 31, v60
	v_lshlrev_b64 v[60:61], 2, v[60:61]
	v_lshl_add_u64 v[74:75], s[14:15], 0, v[60:61]
	v_add_co_u32_e32 v76, vcc, s11, v74
	v_lshl_add_u64 v[60:61], s[6:7], 0, v[60:61]
	s_nop 0
	v_addc_co_u32_e32 v77, vcc, 0, v75, vcc
	v_add_co_u32_e32 v78, vcc, s11, v60
	v_lshl_add_u64 v[62:63], v[82:83], 2, s[12:13]
	s_nop 0
	v_addc_co_u32_e32 v79, vcc, 0, v61, vcc
	v_add_co_u32_e32 v80, vcc, s35, v74
	v_lshl_add_u64 v[64:65], v[62:63], 0, v[100:101]
	s_nop 0
	v_addc_co_u32_e32 v81, vcc, 0, v75, vcc
	v_lshl_add_u64 v[66:67], v[62:63], 0, v[102:103]
	v_lshl_add_u64 v[68:69], v[62:63], 0, v[104:105]
	v_lshl_add_u64 v[70:71], v[62:63], 0, v[106:107]
	v_lshl_add_u64 v[72:73], v[62:63], 0, v[108:109]
	v_lshl_add_u64 v[62:63], v[62:63], 0, v[110:111]
	v_add_co_u32_e32 v82, vcc, s35, v60
	v_ashrrev_i32_e32 v59, 31, v58
	s_nop 0
	v_addc_co_u32_e32 v83, vcc, 0, v61, vcc
	s_andn2_b64 vcc, exec, s[0:1]
	s_mov_b64 s[0:1], -1
	v_pk_add_f32 v[50:51], v[50:51], v[52:53]
	s_nop 0
	v_pk_add_f32 v[26:27], v[50:51], v[26:27]
	v_pk_add_f32 v[30:31], v[50:51], v[30:31]
	v_pk_add_f32 v[52:53], v[54:55], v[56:57]
	v_pk_add_f32 v[34:35], v[50:51], v[34:35]
	v_pk_add_f32 v[28:29], v[52:53], v[28:29]
	v_pk_add_f32 v[38:39], v[50:51], v[38:39]
	v_pk_add_f32 v[42:43], v[50:51], v[42:43]
	v_pk_add_f32 v[46:47], v[50:51], v[46:47]
	v_pk_add_f32 v[32:33], v[52:53], v[32:33]
	v_pk_add_f32 v[36:37], v[52:53], v[36:37]
	v_pk_add_f32 v[40:41], v[52:53], v[40:41]
	v_pk_add_f32 v[44:45], v[52:53], v[44:45]
	v_pk_add_f32 v[48:49], v[52:53], v[48:49]
	global_store_dwordx4 v[64:65], v[26:29], off
	global_store_dwordx4 v[66:67], v[30:33], off
	global_store_dwordx4 v[68:69], v[34:37], off
	global_store_dwordx4 v[70:71], v[38:41], off
	global_store_dwordx4 v[72:73], v[42:45], off
	global_store_dwordx4 v[62:63], v[46:49], off
	v_mov_b32_e32 v26, v242
	v_mov_b32_e32 v28, v244
	v_mov_b32_e32 v27, v243
	v_mov_b32_e32 v30, v246
	v_mov_b32_e32 v29, v245
	v_mov_b32_e32 v32, v248
	v_mov_b32_e32 v31, v247
	v_mov_b32_e32 v33, v249
	v_lshl_add_u64 v[34:35], v[58:59], 2, s[12:13]
	v_lshl_add_u64 v[36:37], v[34:35], 0, v[100:101]
	v_lshl_add_u64 v[38:39], v[34:35], 0, v[102:103]
	v_lshl_add_u64 v[40:41], v[34:35], 0, v[104:105]
	v_lshl_add_u64 v[42:43], v[34:35], 0, v[106:107]
	v_lshl_add_u64 v[44:45], v[34:35], 0, v[108:109]
	v_lshl_add_u64 v[34:35], v[34:35], 0, v[110:111]
	v_pk_add_f32 v[26:27], v[26:27], v[28:29]
	s_nop 0
	v_pk_add_f32 v[2:3], v[26:27], v[2:3]
	v_pk_add_f32 v[6:7], v[26:27], v[6:7]
	v_pk_add_f32 v[28:29], v[30:31], v[32:33]
	v_pk_add_f32 v[10:11], v[26:27], v[10:11]
	v_pk_add_f32 v[4:5], v[28:29], v[4:5]
	v_pk_add_f32 v[14:15], v[26:27], v[14:15]
	v_pk_add_f32 v[18:19], v[26:27], v[18:19]
	v_pk_add_f32 v[22:23], v[26:27], v[22:23]
	v_pk_add_f32 v[8:9], v[28:29], v[8:9]
	v_pk_add_f32 v[12:13], v[28:29], v[12:13]
	v_pk_add_f32 v[16:17], v[28:29], v[16:17]
	v_pk_add_f32 v[20:21], v[28:29], v[20:21]
	v_pk_add_f32 v[24:25], v[28:29], v[24:25]
	global_store_dwordx4 v[36:37], v[2:5], off
	global_store_dwordx4 v[38:39], v[6:9], off
	global_store_dwordx4 v[40:41], v[10:13], off
	global_store_dwordx4 v[42:43], v[14:17], off
	global_store_dwordx4 v[44:45], v[18:21], off
	global_store_dwordx4 v[34:35], v[22:25], off
	s_cbranch_vccnz .LBB4_5
	s_and_saveexec_b64 s[0:1], s[2:3]
	s_cbranch_execz .LBB4_4
	s_barrier
	s_branch .LBB4_4

	.amdhsa_kernel _Z11gemm_8phaseILi0EEvPKDF16_S1_PfPKfS4_
		.amdhsa_group_segment_fixed_size 0
		.amdhsa_private_segment_fixed_size 0
		.amdhsa_kernarg_size 296
		.amdhsa_user_sgpr_count 2
		.amdhsa_user_sgpr_dispatch_ptr 0
		.amdhsa_user_sgpr_queue_ptr 0
		.amdhsa_user_sgpr_kernarg_segment_ptr 1
		.amdhsa_user_sgpr_dispatch_id 0
		.amdhsa_user_sgpr_kernarg_preload_length 0
		.amdhsa_user_sgpr_kernarg_preload_offset 0
		.amdhsa_user_sgpr_private_segment_size 0
		.amdhsa_uses_dynamic_stack 0
		.amdhsa_enable_private_segment 0
		.amdhsa_system_sgpr_workgroup_id_x 1
		.amdhsa_system_sgpr_workgroup_id_y 0
		.amdhsa_system_sgpr_workgroup_id_z 0
		.amdhsa_system_sgpr_workgroup_info 0
		.amdhsa_system_vgpr_workitem_id 0
		.amdhsa_next_free_vgpr 250
		.amdhsa_next_free_sgpr 53
		.amdhsa_accum_offset 252
		.amdhsa_reserve_vcc 1
		.amdhsa_float_round_mode_32 0
		.amdhsa_float_round_mode_16_64 0
		.amdhsa_float_denorm_mode_32 3
		.amdhsa_float_denorm_mode_16_64 3
		.amdhsa_dx10_clamp 1
		.amdhsa_ieee_mode 1
		.amdhsa_fp16_overflow 0
		.amdhsa_tg_split 0
		.amdhsa_exception_fp_ieee_invalid_op 0
		.amdhsa_exception_fp_denorm_src 0
		.amdhsa_exception_fp_ieee_div_zero 0
		.amdhsa_exception_fp_ieee_overflow 0
		.amdhsa_exception_fp_ieee_underflow 0
		.amdhsa_exception_fp_ieee_inexact 0
		.amdhsa_exception_int_div_zero 0
	.end_amdhsa_kernel

amdhsa.kernels:
  - .agpr_count:     0
    .args:
      - .actual_access:  read_only
        .address_space:  global
        .offset:         0
        .size:           8
        .value_kind:     global_buffer
      - .actual_access:  read_only
        .address_space:  global
        .offset:         8
        .size:           8
        .value_kind:     global_buffer
      - .actual_access:  read_only
        .address_space:  global
        .offset:         16
        .size:           8
        .value_kind:     global_buffer
      - .actual_access:  read_only
        .address_space:  global
        .offset:         24
        .size:           8
        .value_kind:     global_buffer
      - .actual_access:  read_only
        .address_space:  global
        .offset:         32
        .size:           8
        .value_kind:     global_buffer
      - .actual_access:  read_only
        .address_space:  global
        .offset:         40
        .size:           8
        .value_kind:     global_buffer
      - .address_space:  global
        .offset:         48
        .size:           8
        .value_kind:     global_buffer
      - .address_space:  global
        .offset:         56
        .size:           8
        .value_kind:     global_buffer
      - .address_space:  global
        .offset:         64
        .size:           8
        .value_kind:     global_buffer
      - .address_space:  global
        .offset:         72
        .size:           8
        .value_kind:     global_buffer
      - .address_space:  global
        .offset:         80
        .size:           8
        .value_kind:     global_buffer
    .group_segment_fixed_size: 0
    .kernarg_segment_align: 8
    .kernarg_segment_size: 88
    .language:       OpenCL C
    .language_version:
      - 2
      - 0
    .max_flat_workgroup_size: 256
    .name:           _Z11prep_kernelPKfPKiS0_S0_S0_S0_PDF16_S3_S3_S3_Pc
    .private_segment_fixed_size: 0
    .sgpr_count:     33
    .sgpr_spill_count: 0
    .symbol:         _Z11prep_kernelPKfPKiS0_S0_S0_S0_PDF16_S3_S3_S3_Pc.kd
    .uniform_work_group_size: 1
    .uses_dynamic_stack: false
    .vgpr_count:     14
    .vgpr_spill_count: 0
    .wavefront_size: 64
  - .agpr_count:     0
    .args:
      - .actual_access:  read_only
        .address_space:  global
        .offset:         0
        .size:           8
        .value_kind:     global_buffer
      - .address_space:  global
        .offset:         8
        .size:           8
        .value_kind:     global_buffer
    .group_segment_fixed_size: 0
    .kernarg_segment_align: 8
    .kernarg_segment_size: 16
    .language:       OpenCL C
    .language_version:
      - 2
      - 0
    .max_flat_workgroup_size: 256
    .name:           _Z7cvt_wfcPKfPDF16_
    .private_segment_fixed_size: 0
    .sgpr_count:     12
    .sgpr_spill_count: 0
    .symbol:         _Z7cvt_wfcPKfPDF16_.kd
    .uniform_work_group_size: 1
    .uses_dynamic_stack: false
    .vgpr_count:     12
    .vgpr_spill_count: 0
    .wavefront_size: 64
  - .agpr_count:     12
    .args:
      - .actual_access:  read_only
        .address_space:  global
        .offset:         0
        .size:           8
        .value_kind:     global_buffer
      - .actual_access:  read_only
        .address_space:  global
        .offset:         8
        .size:           8
        .value_kind:     global_buffer
      - .address_space:  global
        .offset:         16
        .size:           8
        .value_kind:     global_buffer
      - .address_space:  global
        .offset:         24
        .size:           8
        .value_kind:     global_buffer
      - .offset:         32
        .size:           4
        .value_kind:     by_value
    .group_segment_fixed_size: 0
    .kernarg_segment_align: 8
    .kernarg_segment_size: 36
    .language:       OpenCL C
    .language_version:
      - 2
      - 0
    .max_flat_workgroup_size: 256
    .name:           _Z9lstm_stepPKfS0_PDF16_Pfi
    .private_segment_fixed_size: 0
    .sgpr_count:     21
    .sgpr_spill_count: 0
    .symbol:         _Z9lstm_stepPKfS0_PDF16_Pfi.kd
    .uniform_work_group_size: 1
    .uses_dynamic_stack: false
    .vgpr_count:     88
    .vgpr_spill_count: 0
    .wavefront_size: 64
  - .agpr_count:     0
    .args:
      - .actual_access:  read_only
        .address_space:  global
        .offset:         0
        .size:           8
        .value_kind:     global_buffer
      - .actual_access:  read_only
        .address_space:  global
        .offset:         8
        .size:           8
        .value_kind:     global_buffer
      - .address_space:  global
        .offset:         16
        .size:           8
        .value_kind:     global_buffer
      - .address_space:  global
        .offset:         24
        .size:           8
        .value_kind:     global_buffer
      - .address_space:  global
        .offset:         32
        .size:           8
        .value_kind:     global_buffer
      - .actual_access:  read_only
        .address_space:  global
        .offset:         40
        .size:           8
        .value_kind:     global_buffer
      - .address_space:  global
        .offset:         48
        .size:           8
        .value_kind:     global_buffer
    .group_segment_fixed_size: 0
    .kernarg_segment_align: 8
    .kernarg_segment_size: 56
    .language:       OpenCL C
    .language_version:
      - 2
      - 0
    .max_flat_workgroup_size: 512
    .name:           _Z15lstm_persistentPKDF16_PKfPDF16_PjS4_S2_S3_
    .private_segment_fixed_size: 0
    .sgpr_count:     62
    .sgpr_spill_count: 0
    .symbol:         _Z15lstm_persistentPKDF16_PKfPDF16_PjS4_S2_S3_.kd
    .uniform_work_group_size: 1
    .uses_dynamic_stack: false
    .vgpr_count:     242
    .vgpr_spill_count: 0
    .wavefront_size: 64
  - .agpr_count:     0
    .args:
      - .address_space:  global
        .offset:         0
        .size:           8
        .value_kind:     global_buffer
      - .address_space:  global
        .offset:         8
        .size:           8
        .value_kind:     global_buffer
      - .address_space:  global
        .offset:         16
        .size:           8
        .value_kind:     global_buffer
      - .address_space:  global
        .offset:         24
        .size:           8
        .value_kind:     global_buffer
      - .address_space:  global
        .offset:         32
        .size:           8
        .value_kind:     global_buffer
      - .offset:         40
        .size:           4
        .value_kind:     hidden_block_count_x
      - .offset:         44
        .size:           4
        .value_kind:     hidden_block_count_y
      - .offset:         48
        .size:           4
        .value_kind:     hidden_block_count_z
      - .offset:         52
        .size:           2
        .value_kind:     hidden_group_size_x
      - .offset:         54
        .size:           2
        .value_kind:     hidden_group_size_y
      - .offset:         56
        .size:           2
        .value_kind:     hidden_group_size_z
      - .offset:         58
        .size:           2
        .value_kind:     hidden_remainder_x
      - .offset:         60
        .size:           2
        .value_kind:     hidden_remainder_y
      - .offset:         62
        .size:           2
        .value_kind:     hidden_remainder_z
      - .offset:         80
        .size:           8
        .value_kind:     hidden_global_offset_x
      - .offset:         88
        .size:           8
        .value_kind:     hidden_global_offset_y
      - .offset:         96
        .size:           8
        .value_kind:     hidden_global_offset_z
      - .offset:         104
        .size:           2
        .value_kind:     hidden_grid_dims
      - .offset:         160
        .size:           4
        .value_kind:     hidden_dynamic_lds_size
    .group_segment_fixed_size: 0
    .kernarg_segment_align: 8
    .kernarg_segment_size: 296
    .language:       OpenCL C
    .language_version:
      - 2
      - 0
    .max_flat_workgroup_size: 512
    .name:           _Z11gemm_8phaseILi0EEvPKDF16_S1_PfPKfS4_
    .private_segment_fixed_size: 0
    .sgpr_count:     59
    .sgpr_spill_count: 0
    .symbol:         _Z11gemm_8phaseILi0EEvPKDF16_S1_PfPKfS4_.kd
    .uniform_work_group_size: 1
    .uses_dynamic_stack: false
    .vgpr_count:     250
    .vgpr_spill_count: 0
    .wavefront_size: 64
  - .agpr_count:     0
    .args:
      - .address_space:  global
        .offset:         0
        .size:           8
        .value_kind:     global_buffer
      - .address_space:  global
        .offset:         8
        .size:           8
        .value_kind:     global_buffer
      - .address_space:  global
        .offset:         16
        .size:           8
        .value_kind:     global_buffer
      - .address_space:  global
        .offset:         24
        .size:           8
        .value_kind:     global_buffer
      - .address_space:  global
        .offset:         32
        .size:           8
        .value_kind:     global_buffer
      - .offset:         40
        .size:           4
        .value_kind:     hidden_block_count_x
      - .offset:         44
        .size:           4
        .value_kind:     hidden_block_count_y
      - .offset:         48
        .size:           4
        .value_kind:     hidden_block_count_z
      - .offset:         52
        .size:           2
        .value_kind:     hidden_group_size_x
      - .offset:         54
        .size:           2
        .value_kind:     hidden_group_size_y
      - .offset:         56
        .size:           2
        .value_kind:     hidden_group_size_z
      - .offset:         58
        .size:           2
        .value_kind:     hidden_remainder_x
      - .offset:         60
        .size:           2
        .value_kind:     hidden_remainder_y
      - .offset:         62
        .size:           2
        .value_kind:     hidden_remainder_z
      - .offset:         80
        .size:           8
        .value_kind:     hidden_global_offset_x
      - .offset:         88
        .size:           8
        .value_kind:     hidden_global_offset_y
      - .offset:         96
        .size:           8
        .value_kind:     hidden_global_offset_z
      - .offset:         104
        .size:           2
        .value_kind:     hidden_grid_dims
      - .offset:         160
        .size:           4
        .value_kind:     hidden_dynamic_lds_size
    .group_segment_fixed_size: 0
    .kernarg_segment_align: 8
    .kernarg_segment_size: 296
    .language:       OpenCL C
    .language_version:
      - 2
      - 0
    .max_flat_workgroup_size: 512
    .name:           _Z11gemm_8phaseILi1EEvPKDF16_S1_PfPKfS4_
    .private_segment_fixed_size: 0
    .sgpr_count:     44
    .sgpr_spill_count: 0
    .symbol:         _Z11gemm_8phaseILi1EEvPKDF16_S1_PfPKfS4_.kd
    .uniform_work_group_size: 1
    .uses_dynamic_stack: false
    .vgpr_count:     256
    .vgpr_spill_count: 0
    .wavefront_size: 64
